# speedup vs baseline: 1.0241x; 1.0120x over previous
.Lno_karg_touch:
	v_mul_f32_e32 v16, v12, v12
	v_add_f32_e32 v17, 0x3f800000, v12
	v_add_f32_e32 v18, 0x40000000, v12
	v_add_f32_e32 v19, 0x40400000, v12
	v_mul_f32_e32 v17, v17, v17
	v_mul_f32_e32 v18, v18, v18
	v_mul_f32_e32 v19, v19, v19
	v_mul_f32_e32 v20, v8, v16
	v_mul_f32_e32 v24, v9, v16
	v_mul_f32_e32 v21, v8, v17
	v_mul_f32_e32 v25, v9, v17
	v_mul_f32_e32 v22, v8, v18
	v_mul_f32_e32 v26, v9, v18
	v_mul_f32_e32 v23, v8, v19
	v_mul_f32_e32 v27, v9, v19
	v_exp_f32_e32 v20, v20
	v_exp_f32_e32 v21, v21
	v_exp_f32_e32 v22, v22
	v_exp_f32_e32 v23, v23
	v_exp_f32_e32 v24, v24
	v_exp_f32_e32 v25, v25
	v_exp_f32_e32 v26, v26
	v_exp_f32_e32 v27, v27
	v_cvt_pk_f16_f32 v32, v20, v21
	v_cvt_pk_f16_f32 v33, v22, v23
	v_cvt_pk_f16_f32 v64, v24, v25
	v_cvt_pk_f16_f32 v65, v26, v27
	v_add_f32_e32 v16, 0x40800000, v12
	v_add_f32_e32 v17, 0x40a00000, v12
	v_add_f32_e32 v18, 0x40c00000, v12
	v_add_f32_e32 v19, 0x40e00000, v12
	v_mul_f32_e32 v16, v16, v16
	v_mul_f32_e32 v17, v17, v17
	v_mul_f32_e32 v18, v18, v18
	v_mul_f32_e32 v19, v19, v19
	v_mul_f32_e32 v20, v8, v16
	v_mul_f32_e32 v24, v9, v16
	v_mul_f32_e32 v21, v8, v17
	v_mul_f32_e32 v25, v9, v17
	v_mul_f32_e32 v22, v8, v18
	v_mul_f32_e32 v26, v9, v18
	v_mul_f32_e32 v23, v8, v19
	v_mul_f32_e32 v27, v9, v19
	v_exp_f32_e32 v20, v20
	v_exp_f32_e32 v21, v21
	v_exp_f32_e32 v22, v22
	v_exp_f32_e32 v23, v23
	v_exp_f32_e32 v24, v24
	v_exp_f32_e32 v25, v25
	v_exp_f32_e32 v26, v26
	v_exp_f32_e32 v27, v27
	v_cvt_pk_f16_f32 v34, v20, v21
	v_cvt_pk_f16_f32 v35, v22, v23
	v_cvt_pk_f16_f32 v66, v24, v25
	v_cvt_pk_f16_f32 v67, v26, v27
	v_add_f32_e32 v16, 0x42000000, v12
	v_add_f32_e32 v17, 0x42040000, v12
	v_add_f32_e32 v18, 0x42080000, v12
	v_add_f32_e32 v19, 0x420c0000, v12
	v_mul_f32_e32 v16, v16, v16
	v_mul_f32_e32 v17, v17, v17
	v_mul_f32_e32 v18, v18, v18
	v_mul_f32_e32 v19, v19, v19
	v_mul_f32_e32 v20, v8, v16
	v_mul_f32_e32 v24, v9, v16
	v_mul_f32_e32 v21, v8, v17
	v_mul_f32_e32 v25, v9, v17
	v_mul_f32_e32 v22, v8, v18
	v_mul_f32_e32 v26, v9, v18
	v_mul_f32_e32 v23, v8, v19
	v_mul_f32_e32 v27, v9, v19
	v_exp_f32_e32 v20, v20
	v_exp_f32_e32 v21, v21
	v_exp_f32_e32 v22, v22
	v_exp_f32_e32 v23, v23
	v_exp_f32_e32 v24, v24
	v_exp_f32_e32 v25, v25
	v_exp_f32_e32 v26, v26
	v_exp_f32_e32 v27, v27
	v_cvt_pk_f16_f32 v36, v20, v21
	v_cvt_pk_f16_f32 v37, v22, v23
	v_cvt_pk_f16_f32 v68, v24, v25
	v_cvt_pk_f16_f32 v69, v26, v27
	v_add_f32_e32 v16, 0x42100000, v12
	v_add_f32_e32 v17, 0x42140000, v12
	v_add_f32_e32 v18, 0x42180000, v12
	v_add_f32_e32 v19, 0x421c0000, v12
	v_mul_f32_e32 v16, v16, v16
	v_mul_f32_e32 v17, v17, v17
	v_mul_f32_e32 v18, v18, v18
	v_mul_f32_e32 v19, v19, v19
	v_mul_f32_e32 v20, v8, v16
	v_mul_f32_e32 v24, v9, v16
	v_mul_f32_e32 v21, v8, v17
	v_mul_f32_e32 v25, v9, v17
	v_mul_f32_e32 v22, v8, v18
	v_mul_f32_e32 v26, v9, v18
	v_mul_f32_e32 v23, v8, v19
	v_mul_f32_e32 v27, v9, v19
	v_exp_f32_e32 v20, v20
	v_exp_f32_e32 v21, v21
	v_exp_f32_e32 v22, v22
	v_exp_f32_e32 v23, v23
	v_exp_f32_e32 v24, v24
	v_exp_f32_e32 v25, v25
	v_exp_f32_e32 v26, v26
	v_exp_f32_e32 v27, v27
	v_cvt_pk_f16_f32 v38, v20, v21
	v_cvt_pk_f16_f32 v39, v22, v23
	v_cvt_pk_f16_f32 v70, v24, v25
	v_cvt_pk_f16_f32 v71, v26, v27
	v_add_u32_e32 v6, 0x8000, v6
	global_load_dwordx4 v[160:163], v6, s[12:13] offset:0 nt
	global_load_dwordx4 v[164:167], v6, s[12:13] offset:1024 nt
	global_load_dwordx4 v[168:171], v6, s[12:13] offset:2048 nt
	global_load_dwordx4 v[172:175], v6, s[12:13] offset:3072 nt
	v_add_f32_e32 v16, 0x42800000, v12
	v_add_f32_e32 v17, 0x42820000, v12
	v_add_f32_e32 v18, 0x42840000, v12
	v_add_f32_e32 v19, 0x42860000, v12
	v_mul_f32_e32 v16, v16, v16
	v_mul_f32_e32 v17, v17, v17
	v_mul_f32_e32 v18, v18, v18
	v_mul_f32_e32 v19, v19, v19
	v_mul_f32_e32 v20, v8, v16
	v_mul_f32_e32 v24, v9, v16
	v_mul_f32_e32 v21, v8, v17
	v_mul_f32_e32 v25, v9, v17
	v_mul_f32_e32 v22, v8, v18
	v_mul_f32_e32 v26, v9, v18
	v_mul_f32_e32 v23, v8, v19
	v_mul_f32_e32 v27, v9, v19
	v_exp_f32_e32 v20, v20
	v_exp_f32_e32 v21, v21
	v_exp_f32_e32 v22, v22
	v_exp_f32_e32 v23, v23
	v_exp_f32_e32 v24, v24
	v_exp_f32_e32 v25, v25
	v_exp_f32_e32 v26, v26
	v_exp_f32_e32 v27, v27
	v_cvt_pk_f16_f32 v40, v20, v21
	v_cvt_pk_f16_f32 v41, v22, v23
	v_cvt_pk_f16_f32 v72, v24, v25
	v_cvt_pk_f16_f32 v73, v26, v27
	v_add_f32_e32 v16, 0x42880000, v12
	v_add_f32_e32 v17, 0x428a0000, v12
	v_add_f32_e32 v18, 0x428c0000, v12
	v_add_f32_e32 v19, 0x428e0000, v12
	v_mul_f32_e32 v16, v16, v16
	v_mul_f32_e32 v17, v17, v17
	v_mul_f32_e32 v18, v18, v18
	v_mul_f32_e32 v19, v19, v19
	v_mul_f32_e32 v20, v8, v16
	v_mul_f32_e32 v24, v9, v16
	v_mul_f32_e32 v21, v8, v17
	v_mul_f32_e32 v25, v9, v17
	v_mul_f32_e32 v22, v8, v18
	v_mul_f32_e32 v26, v9, v18
	v_mul_f32_e32 v23, v8, v19
	v_mul_f32_e32 v27, v9, v19
	v_exp_f32_e32 v20, v20
	v_exp_f32_e32 v21, v21
	v_exp_f32_e32 v22, v22
	v_exp_f32_e32 v23, v23
	v_exp_f32_e32 v24, v24
	v_exp_f32_e32 v25, v25
	v_exp_f32_e32 v26, v26
	v_exp_f32_e32 v27, v27
	v_cvt_pk_f16_f32 v42, v20, v21
	v_cvt_pk_f16_f32 v43, v22, v23
	v_cvt_pk_f16_f32 v74, v24, v25
	v_cvt_pk_f16_f32 v75, v26, v27
	v_add_f32_e32 v16, 0x42c00000, v12
	v_add_f32_e32 v17, 0x42c20000, v12
	v_add_f32_e32 v18, 0x42c40000, v12
	v_add_f32_e32 v19, 0x42c60000, v12
	v_mul_f32_e32 v16, v16, v16
	v_mul_f32_e32 v17, v17, v17
	v_mul_f32_e32 v18, v18, v18
	v_mul_f32_e32 v19, v19, v19
	v_mul_f32_e32 v20, v8, v16
	v_mul_f32_e32 v24, v9, v16
	v_mul_f32_e32 v21, v8, v17
	v_mul_f32_e32 v25, v9, v17
	v_mul_f32_e32 v22, v8, v18
	v_mul_f32_e32 v26, v9, v18
	v_mul_f32_e32 v23, v8, v19
	v_mul_f32_e32 v27, v9, v19
	v_exp_f32_e32 v20, v20
	v_exp_f32_e32 v21, v21
	v_exp_f32_e32 v22, v22
	v_exp_f32_e32 v23, v23
	v_exp_f32_e32 v24, v24
	v_exp_f32_e32 v25, v25
	v_exp_f32_e32 v26, v26
	v_exp_f32_e32 v27, v27
	v_cvt_pk_f16_f32 v44, v20, v21
	v_cvt_pk_f16_f32 v45, v22, v23
	v_cvt_pk_f16_f32 v76, v24, v25
	v_cvt_pk_f16_f32 v77, v26, v27
	v_add_f32_e32 v16, 0x42c80000, v12
	v_add_f32_e32 v17, 0x42ca0000, v12
	v_add_f32_e32 v18, 0x42cc0000, v12
	v_add_f32_e32 v19, 0x42ce0000, v12
	v_mul_f32_e32 v16, v16, v16
	v_mul_f32_e32 v17, v17, v17
	v_mul_f32_e32 v18, v18, v18
	v_mul_f32_e32 v19, v19, v19
	v_mul_f32_e32 v20, v8, v16
	v_mul_f32_e32 v24, v9, v16
	v_mul_f32_e32 v21, v8, v17
	v_mul_f32_e32 v25, v9, v17
	v_mul_f32_e32 v22, v8, v18
	v_mul_f32_e32 v26, v9, v18
	v_mul_f32_e32 v23, v8, v19
	v_mul_f32_e32 v27, v9, v19
	v_exp_f32_e32 v20, v20
	v_exp_f32_e32 v21, v21
	v_exp_f32_e32 v22, v22
	v_exp_f32_e32 v23, v23
	v_exp_f32_e32 v24, v24
	v_exp_f32_e32 v25, v25
	v_exp_f32_e32 v26, v26
	v_exp_f32_e32 v27, v27
	v_cvt_pk_f16_f32 v46, v20, v21
	v_cvt_pk_f16_f32 v47, v22, v23
	v_cvt_pk_f16_f32 v78, v24, v25
	v_cvt_pk_f16_f32 v79, v26, v27
	v_add_u32_e32 v6, 0x8000, v6
	global_load_dwordx4 v[176:179], v6, s[12:13] offset:0 nt
	global_load_dwordx4 v[180:183], v6, s[12:13] offset:1024 nt
	global_load_dwordx4 v[184:187], v6, s[12:13] offset:2048 nt
	global_load_dwordx4 v[188:191], v6, s[12:13] offset:3072 nt
	v_mul_f32_e32 v16, v2, v2
	v_add_f32_e32 v17, 0x3f800000, v2
	v_add_f32_e32 v18, 0x40000000, v2
	v_add_f32_e32 v19, 0x40400000, v2
	v_mul_f32_e32 v17, v17, v17
	v_mul_f32_e32 v18, v18, v18
	v_mul_f32_e32 v19, v19, v19
	v_mul_f32_e32 v20, v28, v16
	v_mul_f32_e32 v24, v29, v16
	v_mul_f32_e32 v21, v28, v17
	v_mul_f32_e32 v25, v29, v17
	v_mul_f32_e32 v22, v28, v18
	v_mul_f32_e32 v26, v29, v18
	v_mul_f32_e32 v23, v28, v19
	v_mul_f32_e32 v27, v29, v19
	v_exp_f32_e32 v20, v20
	v_exp_f32_e32 v21, v21
	v_exp_f32_e32 v22, v22
	v_exp_f32_e32 v23, v23
	v_exp_f32_e32 v24, v24
	v_exp_f32_e32 v25, v25
	v_exp_f32_e32 v26, v26
	v_exp_f32_e32 v27, v27
	v_cvt_pk_f16_f32 v48, v20, v21
	v_cvt_pk_f16_f32 v49, v22, v23
	v_cvt_pk_f16_f32 v80, v24, v25
	v_cvt_pk_f16_f32 v81, v26, v27
	v_add_f32_e32 v16, 0x40800000, v2
	v_add_f32_e32 v17, 0x40a00000, v2
	v_add_f32_e32 v18, 0x40c00000, v2
	v_add_f32_e32 v19, 0x40e00000, v2
	v_mul_f32_e32 v16, v16, v16
	v_mul_f32_e32 v17, v17, v17
	v_mul_f32_e32 v18, v18, v18
	v_mul_f32_e32 v19, v19, v19
	v_mul_f32_e32 v20, v28, v16
	v_mul_f32_e32 v24, v29, v16
	v_mul_f32_e32 v21, v28, v17
	v_mul_f32_e32 v25, v29, v17
	v_mul_f32_e32 v22, v28, v18
	v_mul_f32_e32 v26, v29, v18
	v_mul_f32_e32 v23, v28, v19
	v_mul_f32_e32 v27, v29, v19
	v_exp_f32_e32 v20, v20
	v_exp_f32_e32 v21, v21
	v_exp_f32_e32 v22, v22
	v_exp_f32_e32 v23, v23
	v_exp_f32_e32 v24, v24
	v_exp_f32_e32 v25, v25
	v_exp_f32_e32 v26, v26
	v_exp_f32_e32 v27, v27
	v_cvt_pk_f16_f32 v50, v20, v21
	v_cvt_pk_f16_f32 v51, v22, v23
	v_cvt_pk_f16_f32 v82, v24, v25
	v_cvt_pk_f16_f32 v83, v26, v27
	v_add_f32_e32 v16, 0x42000000, v2
	v_add_f32_e32 v17, 0x42040000, v2
	v_add_f32_e32 v18, 0x42080000, v2
	v_add_f32_e32 v19, 0x420c0000, v2
	v_mul_f32_e32 v16, v16, v16
	v_mul_f32_e32 v17, v17, v17
	v_mul_f32_e32 v18, v18, v18
	v_mul_f32_e32 v19, v19, v19
	v_mul_f32_e32 v20, v28, v16
	v_mul_f32_e32 v24, v29, v16
	v_mul_f32_e32 v21, v28, v17
	v_mul_f32_e32 v25, v29, v17
	v_mul_f32_e32 v22, v28, v18
	v_mul_f32_e32 v26, v29, v18
	v_mul_f32_e32 v23, v28, v19
	v_mul_f32_e32 v27, v29, v19
	v_exp_f32_e32 v20, v20
	v_exp_f32_e32 v21, v21
	v_exp_f32_e32 v22, v22
	v_exp_f32_e32 v23, v23
	v_exp_f32_e32 v24, v24
	v_exp_f32_e32 v25, v25
	v_exp_f32_e32 v26, v26
	v_exp_f32_e32 v27, v27
	v_cvt_pk_f16_f32 v52, v20, v21
	v_cvt_pk_f16_f32 v53, v22, v23
	v_cvt_pk_f16_f32 v84, v24, v25
	v_cvt_pk_f16_f32 v85, v26, v27
	v_add_f32_e32 v16, 0x42100000, v2
	v_add_f32_e32 v17, 0x42140000, v2
	v_add_f32_e32 v18, 0x42180000, v2
	v_add_f32_e32 v19, 0x421c0000, v2
	v_mul_f32_e32 v16, v16, v16
	v_mul_f32_e32 v17, v17, v17
	v_mul_f32_e32 v18, v18, v18
	v_mul_f32_e32 v19, v19, v19
	v_mul_f32_e32 v20, v28, v16
	v_mul_f32_e32 v24, v29, v16
	v_mul_f32_e32 v21, v28, v17
	v_mul_f32_e32 v25, v29, v17
	v_mul_f32_e32 v22, v28, v18
	v_mul_f32_e32 v26, v29, v18
	v_mul_f32_e32 v23, v28, v19
	v_mul_f32_e32 v27, v29, v19
	v_exp_f32_e32 v20, v20
	v_exp_f32_e32 v21, v21
	v_exp_f32_e32 v22, v22
	v_exp_f32_e32 v23, v23
	v_exp_f32_e32 v24, v24
	v_exp_f32_e32 v25, v25
	v_exp_f32_e32 v26, v26
	v_exp_f32_e32 v27, v27
	v_cvt_pk_f16_f32 v54, v20, v21
	v_cvt_pk_f16_f32 v55, v22, v23
	v_cvt_pk_f16_f32 v86, v24, v25
	v_cvt_pk_f16_f32 v87, v26, v27
	v_add_u32_e32 v6, 0x8000, v6
	global_load_dwordx4 v[192:195], v6, s[12:13] offset:0 nt
	global_load_dwordx4 v[196:199], v6, s[12:13] offset:1024 nt
	global_load_dwordx4 v[200:203], v6, s[12:13] offset:2048 nt
	global_load_dwordx4 v[204:207], v6, s[12:13] offset:3072 nt
	v_add_f32_e32 v16, 0x42800000, v2
	v_add_f32_e32 v17, 0x42820000, v2
	v_add_f32_e32 v18, 0x42840000, v2
	v_add_f32_e32 v19, 0x42860000, v2
	v_mul_f32_e32 v16, v16, v16
	v_mul_f32_e32 v17, v17, v17
	v_mul_f32_e32 v18, v18, v18
	v_mul_f32_e32 v19, v19, v19
	v_mul_f32_e32 v20, v28, v16
	v_mul_f32_e32 v24, v29, v16
	v_mul_f32_e32 v21, v28, v17
	v_mul_f32_e32 v25, v29, v17
	v_mul_f32_e32 v22, v28, v18
	v_mul_f32_e32 v26, v29, v18
	v_mul_f32_e32 v23, v28, v19
	v_mul_f32_e32 v27, v29, v19
	v_exp_f32_e32 v20, v20
	v_exp_f32_e32 v21, v21
	v_exp_f32_e32 v22, v22
	v_exp_f32_e32 v23, v23
	v_exp_f32_e32 v24, v24
	v_exp_f32_e32 v25, v25
	v_exp_f32_e32 v26, v26
	v_exp_f32_e32 v27, v27
	v_cvt_pk_f16_f32 v56, v20, v21
	v_cvt_pk_f16_f32 v57, v22, v23
	v_cvt_pk_f16_f32 v88, v24, v25
	v_cvt_pk_f16_f32 v89, v26, v27
	v_add_f32_e32 v16, 0x42880000, v2
	v_add_f32_e32 v17, 0x428a0000, v2
	v_add_f32_e32 v18, 0x428c0000, v2
	v_add_f32_e32 v19, 0x428e0000, v2
	v_mul_f32_e32 v16, v16, v16
	v_mul_f32_e32 v17, v17, v17
	v_mul_f32_e32 v18, v18, v18
	v_mul_f32_e32 v19, v19, v19
	v_mul_f32_e32 v20, v28, v16
	v_mul_f32_e32 v24, v29, v16
	v_mul_f32_e32 v21, v28, v17
	v_mul_f32_e32 v25, v29, v17
	v_mul_f32_e32 v22, v28, v18
	v_mul_f32_e32 v26, v29, v18
	v_mul_f32_e32 v23, v28, v19
	v_mul_f32_e32 v27, v29, v19
	v_exp_f32_e32 v20, v20
	v_exp_f32_e32 v21, v21
	v_exp_f32_e32 v22, v22
	v_exp_f32_e32 v23, v23
	v_exp_f32_e32 v24, v24
	v_exp_f32_e32 v25, v25
	v_exp_f32_e32 v26, v26
	v_exp_f32_e32 v27, v27
	v_cvt_pk_f16_f32 v58, v20, v21
	v_cvt_pk_f16_f32 v59, v22, v23
	v_cvt_pk_f16_f32 v90, v24, v25
	v_cvt_pk_f16_f32 v91, v26, v27
	v_add_f32_e32 v16, 0x42c00000, v2
	v_add_f32_e32 v17, 0x42c20000, v2
	v_add_f32_e32 v18, 0x42c40000, v2
	v_add_f32_e32 v19, 0x42c60000, v2
	v_mul_f32_e32 v16, v16, v16
	v_mul_f32_e32 v17, v17, v17
	v_mul_f32_e32 v18, v18, v18
	v_mul_f32_e32 v19, v19, v19
	v_mul_f32_e32 v20, v28, v16
	v_mul_f32_e32 v24, v29, v16
	v_mul_f32_e32 v21, v28, v17
	v_mul_f32_e32 v25, v29, v17
	v_mul_f32_e32 v22, v28, v18
	v_mul_f32_e32 v26, v29, v18
	v_mul_f32_e32 v23, v28, v19
	v_mul_f32_e32 v27, v29, v19
	v_exp_f32_e32 v20, v20
	v_exp_f32_e32 v21, v21
	v_exp_f32_e32 v22, v22
	v_exp_f32_e32 v23, v23
	v_exp_f32_e32 v24, v24
	v_exp_f32_e32 v25, v25
	v_exp_f32_e32 v26, v26
	v_exp_f32_e32 v27, v27
	v_cvt_pk_f16_f32 v60, v20, v21
	v_cvt_pk_f16_f32 v61, v22, v23
	v_cvt_pk_f16_f32 v92, v24, v25
	v_cvt_pk_f16_f32 v93, v26, v27
	v_add_f32_e32 v16, 0x42c80000, v2
	v_add_f32_e32 v17, 0x42ca0000, v2
	v_add_f32_e32 v18, 0x42cc0000, v2
	v_add_f32_e32 v19, 0x42ce0000, v2
	v_mul_f32_e32 v16, v16, v16
	v_mul_f32_e32 v17, v17, v17
	v_mul_f32_e32 v18, v18, v18
	v_mul_f32_e32 v19, v19, v19
	v_mul_f32_e32 v20, v28, v16
	v_mul_f32_e32 v24, v29, v16
	v_mul_f32_e32 v21, v28, v17
	v_mul_f32_e32 v25, v29, v17
	v_mul_f32_e32 v22, v28, v18
	v_mul_f32_e32 v26, v29, v18
	v_mul_f32_e32 v23, v28, v19
	v_mul_f32_e32 v27, v29, v19
	v_exp_f32_e32 v20, v20
	v_exp_f32_e32 v21, v21
	v_exp_f32_e32 v22, v22
	v_exp_f32_e32 v23, v23
	v_exp_f32_e32 v24, v24
	v_exp_f32_e32 v25, v25
	v_exp_f32_e32 v26, v26
	v_exp_f32_e32 v27, v27
	v_cvt_pk_f16_f32 v62, v20, v21
	v_cvt_pk_f16_f32 v63, v22, v23
	v_cvt_pk_f16_f32 v94, v24, v25
	v_cvt_pk_f16_f32 v95, v26, v27
	v_add_u32_e32 v6, 0x8000, v6
	global_load_dwordx4 v[208:211], v6, s[12:13] offset:0 nt
	global_load_dwordx4 v[212:215], v6, s[12:13] offset:1024 nt
	global_load_dwordx4 v[216:219], v6, s[12:13] offset:2048 nt
	global_load_dwordx4 v[220:223], v6, s[12:13] offset:3072 nt
	v_mul_f32_e32 v16, v13, v13
	v_add_f32_e32 v17, 0x3f800000, v13
	v_add_f32_e32 v18, 0x40000000, v13
	v_add_f32_e32 v19, 0x40400000, v13
	v_mul_f32_e32 v17, v17, v17
	v_mul_f32_e32 v18, v18, v18
	v_mul_f32_e32 v19, v19, v19
	v_mul_f32_e32 v20, v8, v16
	v_mul_f32_e32 v24, v9, v16
	v_mul_f32_e32 v21, v8, v17
	v_mul_f32_e32 v25, v9, v17
	v_mul_f32_e32 v22, v8, v18
	v_mul_f32_e32 v26, v9, v18
	v_mul_f32_e32 v23, v8, v19
	v_mul_f32_e32 v27, v9, v19
	v_exp_f32_e32 v20, v20
	v_exp_f32_e32 v21, v21
	v_exp_f32_e32 v22, v22
	v_exp_f32_e32 v23, v23
	v_exp_f32_e32 v24, v24
	v_exp_f32_e32 v25, v25
	v_exp_f32_e32 v26, v26
	v_exp_f32_e32 v27, v27
	v_mul_f32_e32 v96, v10, v20
	v_mul_f32_e32 v97, v10, v21
	v_mul_f32_e32 v98, v10, v22
	v_mul_f32_e32 v99, v10, v23
	v_mul_f32_e32 v112, v11, v24
	v_mul_f32_e32 v113, v11, v25
	v_mul_f32_e32 v114, v11, v26
	v_mul_f32_e32 v115, v11, v27
	v_add_f32_e32 v16, 0x41800000, v13
	v_add_f32_e32 v17, 0x41880000, v13
	v_add_f32_e32 v18, 0x41900000, v13
	v_add_f32_e32 v19, 0x41980000, v13
	v_mul_f32_e32 v16, v16, v16
	v_mul_f32_e32 v17, v17, v17
	v_mul_f32_e32 v18, v18, v18
	v_mul_f32_e32 v19, v19, v19
	v_mul_f32_e32 v20, v8, v16
	v_mul_f32_e32 v24, v9, v16
	v_mul_f32_e32 v21, v8, v17
	v_mul_f32_e32 v25, v9, v17
	v_mul_f32_e32 v22, v8, v18
	v_mul_f32_e32 v26, v9, v18
	v_mul_f32_e32 v23, v8, v19
	v_mul_f32_e32 v27, v9, v19
	v_exp_f32_e32 v20, v20
	v_exp_f32_e32 v21, v21
	v_exp_f32_e32 v22, v22
	v_exp_f32_e32 v23, v23
	v_exp_f32_e32 v24, v24
	v_exp_f32_e32 v25, v25
	v_exp_f32_e32 v26, v26
	v_exp_f32_e32 v27, v27
	v_mul_f32_e32 v100, v10, v20
	v_mul_f32_e32 v101, v10, v21
	v_mul_f32_e32 v102, v10, v22
	v_mul_f32_e32 v103, v10, v23
	v_mul_f32_e32 v116, v11, v24
	v_mul_f32_e32 v117, v11, v25
	v_mul_f32_e32 v118, v11, v26
	v_mul_f32_e32 v119, v11, v27
	v_mul_f32_e32 v16, v3, v3
	v_add_f32_e32 v17, 0x3f800000, v3
	v_add_f32_e32 v18, 0x40000000, v3
	v_add_f32_e32 v19, 0x40400000, v3
	v_mul_f32_e32 v17, v17, v17
	v_mul_f32_e32 v18, v18, v18
	v_mul_f32_e32 v19, v19, v19
	v_mul_f32_e32 v20, v28, v16
	v_mul_f32_e32 v24, v29, v16
	v_mul_f32_e32 v21, v28, v17
	v_mul_f32_e32 v25, v29, v17
	v_mul_f32_e32 v22, v28, v18
	v_mul_f32_e32 v26, v29, v18
	v_mul_f32_e32 v23, v28, v19
	v_mul_f32_e32 v27, v29, v19
	v_exp_f32_e32 v20, v20
	v_exp_f32_e32 v21, v21
	v_exp_f32_e32 v22, v22
	v_exp_f32_e32 v23, v23
	v_exp_f32_e32 v24, v24
	v_exp_f32_e32 v25, v25
	v_exp_f32_e32 v26, v26
	v_exp_f32_e32 v27, v27
	v_mul_f32_e32 v104, v30, v20
	v_mul_f32_e32 v105, v30, v21
	v_mul_f32_e32 v106, v30, v22
	v_mul_f32_e32 v107, v30, v23
	v_mul_f32_e32 v120, v31, v24
	v_mul_f32_e32 v121, v31, v25
	v_mul_f32_e32 v122, v31, v26
	v_mul_f32_e32 v123, v31, v27
	v_add_f32_e32 v16, 0x41800000, v3
	v_add_f32_e32 v17, 0x41880000, v3
	v_add_f32_e32 v18, 0x41900000, v3
	v_add_f32_e32 v19, 0x41980000, v3
	v_mul_f32_e32 v16, v16, v16
	v_mul_f32_e32 v17, v17, v17
	v_mul_f32_e32 v18, v18, v18
	v_mul_f32_e32 v19, v19, v19
	v_mul_f32_e32 v20, v28, v16
	v_mul_f32_e32 v24, v29, v16
	v_mul_f32_e32 v21, v28, v17
	v_mul_f32_e32 v25, v29, v17
	v_mul_f32_e32 v22, v28, v18
	v_mul_f32_e32 v26, v29, v18
	v_mul_f32_e32 v23, v28, v19
	v_mul_f32_e32 v27, v29, v19
	v_exp_f32_e32 v20, v20
	v_exp_f32_e32 v21, v21
	v_exp_f32_e32 v22, v22
	v_exp_f32_e32 v23, v23
	v_exp_f32_e32 v24, v24
	v_exp_f32_e32 v25, v25
	v_exp_f32_e32 v26, v26
	v_exp_f32_e32 v27, v27
	v_mul_f32_e32 v108, v30, v20
	v_mul_f32_e32 v109, v30, v21
	v_mul_f32_e32 v110, v30, v22
	v_mul_f32_e32 v111, v30, v23
	v_mul_f32_e32 v124, v31, v24
	v_mul_f32_e32 v125, v31, v25
	v_mul_f32_e32 v126, v31, v26
	v_mul_f32_e32 v127, v31, v27
	v_add_u32_e32 v6, 0x8000, v6
	global_load_dwordx4 v[224:227], v6, s[12:13] offset:0 nt
	global_load_dwordx4 v[228:231], v6, s[12:13] offset:1024 nt
	global_load_dwordx4 v[232:235], v6, s[12:13] offset:2048 nt
	global_load_dwordx4 v[236:239], v6, s[12:13] offset:3072 nt
	s_waitcnt vmcnt(24)
	v_add_f32_e32 v128, v128, v129
	v_add_f32_e32 v130, v130, v131
	v_add_f32_e32 v132, v132, v133
	v_add_f32_e32 v134, v134, v135
	v_add_f32_e32 v136, v136, v137
	v_add_f32_e32 v138, v138, v139
	v_add_f32_e32 v140, v140, v141
	v_add_f32_e32 v142, v142, v143
	v_add_f32_e32 v128, v128, v130
	v_add_f32_e32 v132, v132, v134
	v_add_f32_e32 v136, v136, v138
	v_add_f32_e32 v140, v140, v142
	v_cndmask_b32_e64 v130, v128, v132, s[30:31]
	v_cndmask_b32_e64 v134, v136, v140, s[30:31]
	v_cndmask_b32_e64 v129, v132, v128, s[30:31]
	v_cndmask_b32_e64 v133, v140, v136, s[30:31]
	v_add_f32_dpp v129, v130, v129 quad_perm:[1,0,3,2] row_mask:0xf bank_mask:0xf bound_ctrl:1
	v_add_f32_dpp v133, v134, v133 quad_perm:[1,0,3,2] row_mask:0xf bank_mask:0xf bound_ctrl:1
	v_cndmask_b32_e64 v135, v129, v133, s[32:33]
	v_cndmask_b32_e64 v131, v133, v129, s[32:33]
	s_nop 1
	v_add_f32_dpp v131, v135, v131 quad_perm:[2,3,0,1] row_mask:0xf bank_mask:0xf bound_ctrl:1
	v_cvt_f16_f32_e32 v131, v131
	ds_write_b16 v14, v131 offset:0
	s_waitcnt vmcnt(20)
	v_add_f32_e32 v144, v144, v145
	v_add_f32_e32 v146, v146, v147
	v_add_f32_e32 v148, v148, v149
	v_add_f32_e32 v150, v150, v151
	v_add_f32_e32 v152, v152, v153
	v_add_f32_e32 v154, v154, v155
	v_add_f32_e32 v156, v156, v157
	v_add_f32_e32 v158, v158, v159
	v_add_f32_e32 v144, v144, v146
	v_add_f32_e32 v148, v148, v150
	v_add_f32_e32 v152, v152, v154
	v_add_f32_e32 v156, v156, v158
	v_cndmask_b32_e64 v146, v144, v148, s[30:31]
	v_cndmask_b32_e64 v150, v152, v156, s[30:31]
	v_cndmask_b32_e64 v145, v148, v144, s[30:31]
	v_cndmask_b32_e64 v149, v156, v152, s[30:31]
	v_add_f32_dpp v145, v146, v145 quad_perm:[1,0,3,2] row_mask:0xf bank_mask:0xf bound_ctrl:1
	v_add_f32_dpp v149, v150, v149 quad_perm:[1,0,3,2] row_mask:0xf bank_mask:0xf bound_ctrl:1
	v_cndmask_b32_e64 v151, v145, v149, s[32:33]
	v_cndmask_b32_e64 v147, v149, v145, s[32:33]
	s_nop 1
	v_add_f32_dpp v147, v151, v147 quad_perm:[2,3,0,1] row_mask:0xf bank_mask:0xf bound_ctrl:1
	v_cvt_f16_f32_e32 v147, v147
	ds_write_b16 v14, v147 offset:1088
	s_waitcnt vmcnt(16)
	v_add_f32_e32 v160, v160, v161
	v_add_f32_e32 v162, v162, v163
	v_add_f32_e32 v164, v164, v165
	v_add_f32_e32 v166, v166, v167
	v_add_f32_e32 v168, v168, v169
	v_add_f32_e32 v170, v170, v171
	v_add_f32_e32 v172, v172, v173
	v_add_f32_e32 v174, v174, v175
	v_add_f32_e32 v160, v160, v162
	v_add_f32_e32 v164, v164, v166
	v_add_f32_e32 v168, v168, v170
	v_add_f32_e32 v172, v172, v174
	v_cndmask_b32_e64 v162, v160, v164, s[30:31]
	v_cndmask_b32_e64 v166, v168, v172, s[30:31]
	v_cndmask_b32_e64 v161, v164, v160, s[30:31]
	v_cndmask_b32_e64 v165, v172, v168, s[30:31]
	v_add_f32_dpp v161, v162, v161 quad_perm:[1,0,3,2] row_mask:0xf bank_mask:0xf bound_ctrl:1
	v_add_f32_dpp v165, v166, v165 quad_perm:[1,0,3,2] row_mask:0xf bank_mask:0xf bound_ctrl:1
	v_cndmask_b32_e64 v167, v161, v165, s[32:33]
	v_cndmask_b32_e64 v163, v165, v161, s[32:33]
	s_nop 1
	v_add_f32_dpp v163, v167, v163 quad_perm:[2,3,0,1] row_mask:0xf bank_mask:0xf bound_ctrl:1
	v_cvt_f16_f32_e32 v163, v163
	ds_write_b16 v14, v163 offset:2176
	s_waitcnt vmcnt(12)
	v_add_f32_e32 v176, v176, v177
	v_add_f32_e32 v178, v178, v179
	v_add_f32_e32 v180, v180, v181
	v_add_f32_e32 v182, v182, v183
	v_add_f32_e32 v184, v184, v185
	v_add_f32_e32 v186, v186, v187
	v_add_f32_e32 v188, v188, v189
	v_add_f32_e32 v190, v190, v191
	v_add_f32_e32 v176, v176, v178
	v_add_f32_e32 v180, v180, v182
	v_add_f32_e32 v184, v184, v186
	v_add_f32_e32 v188, v188, v190
	v_cndmask_b32_e64 v178, v176, v180, s[30:31]
	v_cndmask_b32_e64 v182, v184, v188, s[30:31]
	v_cndmask_b32_e64 v177, v180, v176, s[30:31]
	v_cndmask_b32_e64 v181, v188, v184, s[30:31]
	v_add_f32_dpp v177, v178, v177 quad_perm:[1,0,3,2] row_mask:0xf bank_mask:0xf bound_ctrl:1
	v_add_f32_dpp v181, v182, v181 quad_perm:[1,0,3,2] row_mask:0xf bank_mask:0xf bound_ctrl:1
	v_cndmask_b32_e64 v183, v177, v181, s[32:33]
	v_cndmask_b32_e64 v179, v181, v177, s[32:33]
	s_nop 1
	v_add_f32_dpp v179, v183, v179 quad_perm:[2,3,0,1] row_mask:0xf bank_mask:0xf bound_ctrl:1
	v_cvt_f16_f32_e32 v179, v179
	ds_write_b16 v14, v179 offset:3264
	s_mov_b32 s29, 0
	v_mov_b32_e32 v160, 0
	v_mov_b32_e32 v161, 0
	v_mov_b32_e32 v162, 0
	v_mov_b32_e32 v163, 0
	s_lshl_b32 s6, s6, 6
	s_add_i32 s6, s6, s7
	s_lshl_b32 s6, s6, 10
	v_add_u32_e32 v5, s6, v5
	s_branch .Lpass
.Lsecond_half:
	v_add_u32_e32 v6, 0x8000, v6
	global_load_dwordx4 v[240:243], v6, s[12:13] offset:0 nt
	global_load_dwordx4 v[244:247], v6, s[12:13] offset:1024 nt
	global_load_dwordx4 v[248:251], v6, s[12:13] offset:2048 nt
	global_load_dwordx4 v[252:255], v6, s[12:13] offset:3072 nt
	s_waitcnt vmcnt(12)
	v_add_f32_e32 v192, v192, v193
	v_add_f32_e32 v194, v194, v195
	v_add_f32_e32 v196, v196, v197
	v_add_f32_e32 v198, v198, v199
	v_add_f32_e32 v200, v200, v201
	v_add_f32_e32 v202, v202, v203
	v_add_f32_e32 v204, v204, v205
	v_add_f32_e32 v206, v206, v207
	v_add_f32_e32 v192, v192, v194
	v_add_f32_e32 v196, v196, v198
	v_add_f32_e32 v200, v200, v202
	v_add_f32_e32 v204, v204, v206
	v_cndmask_b32_e64 v194, v192, v196, s[30:31]
	v_cndmask_b32_e64 v198, v200, v204, s[30:31]
	v_cndmask_b32_e64 v193, v196, v192, s[30:31]
	v_cndmask_b32_e64 v197, v204, v200, s[30:31]
	v_add_f32_dpp v193, v194, v193 quad_perm:[1,0,3,2] row_mask:0xf bank_mask:0xf bound_ctrl:1
	v_add_f32_dpp v197, v198, v197 quad_perm:[1,0,3,2] row_mask:0xf bank_mask:0xf bound_ctrl:1
	v_cndmask_b32_e64 v199, v193, v197, s[32:33]
	v_cndmask_b32_e64 v195, v197, v193, s[32:33]
	s_nop 1
	v_add_f32_dpp v195, v199, v195 quad_perm:[2,3,0,1] row_mask:0xf bank_mask:0xf bound_ctrl:1
	v_cvt_f16_f32_e32 v195, v195
	ds_write_b16 v14, v195 offset:4352
	s_waitcnt vmcnt(8)
	v_add_f32_e32 v208, v208, v209
	v_add_f32_e32 v210, v210, v211
	v_add_f32_e32 v212, v212, v213
	v_add_f32_e32 v214, v214, v215
	v_add_f32_e32 v216, v216, v217
	v_add_f32_e32 v218, v218, v219
	v_add_f32_e32 v220, v220, v221
	v_add_f32_e32 v222, v222, v223
	v_add_f32_e32 v208, v208, v210
	v_add_f32_e32 v212, v212, v214
	v_add_f32_e32 v216, v216, v218
	v_add_f32_e32 v220, v220, v222
	v_cndmask_b32_e64 v210, v208, v212, s[30:31]
	v_cndmask_b32_e64 v214, v216, v220, s[30:31]
	v_cndmask_b32_e64 v209, v212, v208, s[30:31]
	v_cndmask_b32_e64 v213, v220, v216, s[30:31]
	v_add_f32_dpp v209, v210, v209 quad_perm:[1,0,3,2] row_mask:0xf bank_mask:0xf bound_ctrl:1
	v_add_f32_dpp v213, v214, v213 quad_perm:[1,0,3,2] row_mask:0xf bank_mask:0xf bound_ctrl:1
	v_cndmask_b32_e64 v215, v209, v213, s[32:33]
	v_cndmask_b32_e64 v211, v213, v209, s[32:33]
	s_nop 1
	v_add_f32_dpp v211, v215, v211 quad_perm:[2,3,0,1] row_mask:0xf bank_mask:0xf bound_ctrl:1
	v_cvt_f16_f32_e32 v211, v211
	ds_write_b16 v14, v211 offset:5440
	s_waitcnt vmcnt(4)
	v_add_f32_e32 v224, v224, v225
	v_add_f32_e32 v226, v226, v227
	v_add_f32_e32 v228, v228, v229
	v_add_f32_e32 v230, v230, v231
	v_add_f32_e32 v232, v232, v233
	v_add_f32_e32 v234, v234, v235
	v_add_f32_e32 v236, v236, v237
	v_add_f32_e32 v238, v238, v239
	v_add_f32_e32 v224, v224, v226
	v_add_f32_e32 v228, v228, v230
	v_add_f32_e32 v232, v232, v234
	v_add_f32_e32 v236, v236, v238
	v_cndmask_b32_e64 v226, v224, v228, s[30:31]
	v_cndmask_b32_e64 v230, v232, v236, s[30:31]
	v_cndmask_b32_e64 v225, v228, v224, s[30:31]
	v_cndmask_b32_e64 v229, v236, v232, s[30:31]
	v_add_f32_dpp v225, v226, v225 quad_perm:[1,0,3,2] row_mask:0xf bank_mask:0xf bound_ctrl:1
	v_add_f32_dpp v229, v230, v229 quad_perm:[1,0,3,2] row_mask:0xf bank_mask:0xf bound_ctrl:1
	v_cndmask_b32_e64 v231, v225, v229, s[32:33]
	v_cndmask_b32_e64 v227, v229, v225, s[32:33]
	s_nop 1
	v_add_f32_dpp v227, v231, v227 quad_perm:[2,3,0,1] row_mask:0xf bank_mask:0xf bound_ctrl:1
	v_cvt_f16_f32_e32 v227, v227
	ds_write_b16 v14, v227 offset:6528
	s_waitcnt vmcnt(0)
	v_add_f32_e32 v240, v240, v241
	v_add_f32_e32 v242, v242, v243
	v_add_f32_e32 v244, v244, v245
	v_add_f32_e32 v246, v246, v247
	v_add_f32_e32 v248, v248, v249
	v_add_f32_e32 v250, v250, v251
	v_add_f32_e32 v252, v252, v253
	v_add_f32_e32 v254, v254, v255
	v_add_f32_e32 v240, v240, v242
	v_add_f32_e32 v244, v244, v246
	v_add_f32_e32 v248, v248, v250
	v_add_f32_e32 v252, v252, v254
	v_cndmask_b32_e64 v242, v240, v244, s[30:31]
	v_cndmask_b32_e64 v246, v248, v252, s[30:31]
	v_cndmask_b32_e64 v241, v244, v240, s[30:31]
	v_cndmask_b32_e64 v245, v252, v248, s[30:31]
	v_add_f32_dpp v241, v242, v241 quad_perm:[1,0,3,2] row_mask:0xf bank_mask:0xf bound_ctrl:1
	v_add_f32_dpp v245, v246, v245 quad_perm:[1,0,3,2] row_mask:0xf bank_mask:0xf bound_ctrl:1
	v_cndmask_b32_e64 v247, v241, v245, s[32:33]
	v_cndmask_b32_e64 v243, v245, v241, s[32:33]
	s_nop 1
	v_add_f32_dpp v243, v247, v243 quad_perm:[2,3,0,1] row_mask:0xf bank_mask:0xf bound_ctrl:1
	v_cvt_f16_f32_e32 v243, v243
	ds_write_b16 v14, v243 offset:7616
